# 3-tile blocks no longer re-read their last row tile for the missing fourth tile (out-of-range zero fill instead)
# speedup vs baseline: 1.0060x; 1.0038x over previous
.Lsteady_w1:
	s_waitcnt vmcnt(19)
	v_cvt_pk_f16_f32 v234, v142, v143
	v_cvt_pk_f16_f32 v235, v144, v145
	v_or_b32_e32 v236, s38, v202
	ds_write_b64 v236, v[234:235]
	v_bfe_u32 v234, v205, s53, 1
	v_cmp_eq_u32_e32 vcc, 0, v234
	v_lshrrev_b32_e32 v241, s53, v205
	s_waitcnt vmcnt(18)
	v_cvt_pk_f16_f32 v236, v138, v139
	v_cndmask_b32_e64 v234, 1.0, 0, vcc
	v_pk_fma_f32 v[142:143], v[234:235], v[142:143], 0 op_sel_hi:[0,1,0]
	v_cvt_pk_f16_f32 v237, v140, v141
	v_or_b32_e32 v235, s38, v201
	ds_write_b64 v235, v[236:237] offset:4096
	v_and_b32_e32 v235, 2, v241
	v_cmp_eq_u32_e32 vcc, 0, v235
	s_add_i32 s52, s41, 7
	s_nop 0
	v_cndmask_b32_e64 v236, 1.0, 0, vcc
	v_pk_fma_f32 v[238:239], v[236:237], v[138:139], v[142:143] op_sel_hi:[0,1,1]
	v_xor_b32_e32 v215, 32, v215
	s_waitcnt lgkmcnt(6)
	v_mfma_f32_32x32x16_f16 v[2:17], v[118:121], v[208:211], v[2:17]
	v_add_u32_e32 v207, v207, v215
	v_fma_f32 v138, v234, v144, 0
	v_fma_f32 v139, v234, v145, 0
	s_waitcnt lgkmcnt(5)
	v_mfma_f32_32x32x16_f16 v[34:49], v[118:121], v[216:219], v[34:49]
	s_waitcnt lgkmcnt(4)
	v_mfma_f32_32x32x16_f16 v[50:65], v[118:121], v[220:223], v[50:65]
	v_fma_f32 v220, v236, v140, v138
	v_fma_f32 v221, v236, v141, v139
	v_add_u32_e32 v254, v240, v215
	s_waitcnt lgkmcnt(3)
	v_mfma_f32_32x32x16_f16 v[18:33], v[118:121], v[226:229], v[18:33]
	ds_read_b128 v[118:121], v207
	ds_read_b128 v[250:253], v207 offset:16384
	ds_read_b128 v[208:211], v207 offset:32768
	ds_read_b128 v[216:219], v207 offset:49152
	ds_read_b128 v[234:237], v254
	s_waitcnt lgkmcnt(7)
	v_mfma_f32_32x32x16_f16 v[66:81], v[114:117], v[230:233], v[66:81]
	s_bfe_u32 s38, s52, 0x10002
	s_lshl_b32 s53, s38, 16
	s_or_b32 s49, s53, s49
	s_waitcnt vmcnt(17)
	v_cvt_pk_f16_f32 v114, v134, v135
	v_cvt_pk_f16_f32 v115, v136, v137
	v_or_b32_e32 v116, s49, v202
	ds_write_b64 v116, v[114:115] offset:8192
	v_and_b32_e32 v114, 4, v241
	v_cmp_eq_u32_e32 vcc, 0, v114
	s_lshl_b32 s38, s38, 14
	s_nop 0
	v_cndmask_b32_e64 v114, 1.0, 0, vcc
	v_pk_fma_f32 v[116:117], v[114:115], v[134:135], v[238:239] op_sel_hi:[0,1,1]
	v_pk_fma_f32 v[114:115], v[114:115], v[136:137], v[220:221] op_sel_hi:[0,1,1]
	s_waitcnt vmcnt(16)
	v_cvt_pk_f16_f32 v134, v130, v131
	v_cvt_pk_f16_f32 v135, v132, v133
	v_or_b32_e32 v136, s49, v201
	s_lshl_b32 s49, s51, 12
	ds_write_b64 v136, v[134:135] offset:12288
	v_and_b32_e32 v134, 8, v241
	s_or_b32 s38, s38, s49
	v_cmp_eq_u32_e32 vcc, 0, v134
	s_bitcmp0_b32 s21, 0
	s_nop 0
	v_cndmask_b32_e64 v134, 1.0, 0, vcc
	s_cselect_b64 vcc, -1, 0
	v_pk_fma_f32 v[116:117], v[134:135], v[130:131], v[116:117] op_sel_hi:[0,1,1]
	v_pk_fma_f32 v[114:115], v[134:135], v[132:133], v[114:115] op_sel_hi:[0,1,1]
	v_cndmask_b32_e32 v207, v201, v202, vcc
	v_cvt_pk_f16_f32 v116, v116, v117
	v_cvt_pk_f16_f32 v117, v114, v115
	v_or_b32_e32 v114, s38, v207
	v_or_b32_e32 v114, 0x20000, v114
	ds_write_b64 v114, v[116:117]
	s_add_i32 s75, s21, 7
	s_and_b32 s76, s75, 3
	s_cmp_gt_u32 s76, s46
	s_cselect_b32 s77, 2.0, 0
	s_lshr_b32 s75, s75, 2
	s_add_i32 s75, s75, s44
	s_min_u32 s76, s76, s46
	s_lshl_b32 s75, s75, 10
	s_and_b32 s75, s75, 0x1c00
	s_lshl_b32 s76, s76, 18
	s_or_b32 s75, s75, s76
	s_cmp_lt_u32 s21, 25
	s_cselect_b32 s76, 0, 2.0
	s_or_b32 s76, s76, s77
	v_add_u32_e32 v130, s76, v197
	v_add_u32_e32 v131, s76, v198
	v_add_u32_e32 v132, s76, v199
	v_add_u32_e32 v133, s76, v200
	buffer_load_dwordx4 v[142:145], v130, s[4:7], s75 offen sc0 nt sc1
	buffer_load_dwordx4 v[138:141], v131, s[4:7], s75 offen sc0 nt sc1
	buffer_load_dwordx4 v[134:137], v132, s[4:7], s75 offen sc0 nt sc1
	buffer_load_dwordx4 v[130:133], v133, s[4:7], s75 offen sc0 nt sc1
	s_waitcnt lgkmcnt(7)
	v_mfma_f32_32x32x16_f16 v[2:17], v[90:93], v[118:121], v[2:17]
	s_waitcnt lgkmcnt(6)
	v_mfma_f32_32x32x16_f16 v[34:49], v[90:93], v[250:253], v[34:49]
	s_waitcnt lgkmcnt(5)
	v_mfma_f32_32x32x16_f16 v[50:65], v[90:93], v[208:211], v[50:65]
	s_waitcnt lgkmcnt(4)
	v_mfma_f32_32x32x16_f16 v[18:33], v[90:93], v[216:219], v[18:33]
	s_waitcnt lgkmcnt(3)
	v_mfma_f32_32x32x16_f16 v[66:81], v[98:101], v[234:237], v[66:81]
	s_cmp_lg_u32 s51, 3
	s_cbranch_scc1 .LBB1_10
	s_waitcnt lgkmcnt(0)
	s_barrier
.LBB1_10:
	s_add_i32 s38, s41, 6
	s_lshr_b32 s38, s38, 2
	s_add_i32 s38, s38, s44
	s_lshl_b32 s38, s38, 17
	s_add_i32 s49, s20, 0xc000
	s_and_b32 s38, s38, 0xe0000
	s_and_b32 s53, s49, 0xc000
	s_or_b32 s38, s38, s53
	v_lshl_add_u64 v[90:91], v[194:195], 0, s[38:39]
	s_add_i32 s38, s41, 10
	s_and_b32 s53, s38, 3
	s_lshr_b32 s38, s38, 2
	s_add_i32 s38, s38, s44
	v_add_co_u32_e32 v92, vcc, 0x1000, v90
	s_min_u32 s53, s53, s46
	s_lshl_b32 s38, s38, 10
	v_addc_co_u32_e32 v93, vcc, 0, v91, vcc
	s_and_b32 s38, s38, 0x1c00
	s_lshl_b32 s53, s53, 18
	global_load_dwordx4 v[118:121], v[90:91], off
	global_load_dwordx4 v[114:117], v[92:93], off
	v_add_co_u32_e32 v92, vcc, 0x2000, v90
	s_or_b32 s38, s38, s53
	s_nop 0
	v_addc_co_u32_e32 v93, vcc, 0, v91, vcc
	s_cmp_lt_u32 s21, 25
	v_add_co_u32_e32 v98, vcc, 0x3000, v90
	s_cselect_b32 s53, 0, 2.0
	s_nop 0
	v_addc_co_u32_e32 v99, vcc, 0, v91, vcc
	global_load_dwordx4 v[90:93], v[92:93], off
	s_nop 0
	global_load_dwordx4 v[98:101], v[98:99], off
	s_nop 0
	s_nop 0
	s_add_i32 s38, s41, 4
	s_bfe_u32 s53, s38, 0x10002
	s_and_b32 s38, s38, 3
	s_lshl_b32 s54, s38, 6
	v_lshl_or_b32 v215, s53, 16, v204
	v_xor_b32_e32 v240, s54, v203
	v_add_u32_e32 v226, v215, v240
	ds_read_b128 v[208:211], v226
	ds_read_b128 v[216:219], v226 offset:16384
	ds_read_b128 v[220:223], v226 offset:32768
	ds_read_b128 v[226:229], v226 offset:49152
	v_lshl_add_u32 v241, s53, 14, v206
	v_add_u32_e32 v230, v241, v240
	ds_read_b128 v[230:233], v230
	s_add_i32 s53, s41, 8
	s_and_b32 s54, s53, 3
	s_add_i32 s55, s20, 0x14000
	s_and_b32 s55, s55, 0x10000
	s_lshl_b32 s56, s54, 14
	s_or_b32 s55, s55, s56
	s_lshl_b32 s57, s54, 2
	s_waitcnt vmcnt(19)
	v_cvt_pk_f16_f32 v234, v126, v127
	v_cvt_pk_f16_f32 v235, v128, v129
	v_or_b32_e32 v236, s55, v202
	ds_write_b64 v236, v[234:235]
	v_bfe_u32 v234, v205, s57, 1
	v_cmp_eq_u32_e32 vcc, 0, v234
	v_lshrrev_b32_e32 v242, s57, v205
	s_waitcnt vmcnt(18)
	v_cvt_pk_f16_f32 v236, v122, v123
	v_cndmask_b32_e64 v234, 1.0, 0, vcc
	v_pk_fma_f32 v[126:127], v[234:235], v[126:127], 0 op_sel_hi:[0,1,0]
	v_cvt_pk_f16_f32 v237, v124, v125
	v_or_b32_e32 v235, s55, v201
	ds_write_b64 v235, v[236:237] offset:4096
	v_and_b32_e32 v235, 2, v242
	v_cmp_eq_u32_e32 vcc, 0, v235
	s_nop 1
	v_cndmask_b32_e64 v236, 1.0, 0, vcc
	v_pk_fma_f32 v[238:239], v[236:237], v[122:123], v[126:127] op_sel_hi:[0,1,1]
	s_waitcnt lgkmcnt(4)
	v_mfma_f32_32x32x16_f16 v[50:65], v[102:105], v[220:223], v[50:65]
	v_xor_b32_e32 v222, 32, v240
	v_add_u32_e32 v215, v215, v222
	v_fma_f32 v122, v234, v128, 0
	v_fma_f32 v123, v234, v129, 0
	v_fma_f32 v220, v236, v124, v122
	v_fma_f32 v221, v236, v125, v123
	v_add_u32_e32 v254, v241, v222
	v_mfma_f32_32x32x16_f16 v[2:17], v[102:105], v[208:211], v[2:17]
	v_mfma_f32_32x32x16_f16 v[34:49], v[102:105], v[216:219], v[34:49]
	s_waitcnt lgkmcnt(3)
	v_mfma_f32_32x32x16_f16 v[18:33], v[102:105], v[226:229], v[18:33]
	ds_read_b128 v[102:105], v215
	ds_read_b128 v[250:253], v215 offset:16384
	ds_read_b128 v[208:211], v215 offset:32768
	ds_read_b128 v[216:219], v215 offset:49152
	ds_read_b128 v[234:237], v254
	s_waitcnt lgkmcnt(7)
	v_mfma_f32_32x32x16_f16 v[66:81], v[94:97], v[230:233], v[66:81]
	s_bfe_u32 s55, s53, 0x10002
	s_lshl_b32 s57, s55, 16
	s_or_b32 s56, s57, s56
	s_waitcnt vmcnt(17)
	v_cvt_pk_f16_f32 v94, v110, v111
	v_cvt_pk_f16_f32 v95, v112, v113
	v_or_b32_e32 v96, s56, v202
	ds_write_b64 v96, v[94:95] offset:8192
	v_and_b32_e32 v94, 4, v242
	v_cmp_eq_u32_e32 vcc, 0, v94
	s_lshl_b32 s55, s55, 14
	s_lshl_b32 s54, s54, 12
	v_cndmask_b32_e64 v94, 1.0, 0, vcc
	v_pk_fma_f32 v[96:97], v[94:95], v[110:111], v[238:239] op_sel_hi:[0,1,1]
	v_pk_fma_f32 v[94:95], v[94:95], v[112:113], v[220:221] op_sel_hi:[0,1,1]
	s_waitcnt vmcnt(16)
	v_cvt_pk_f16_f32 v110, v106, v107
	v_cvt_pk_f16_f32 v111, v108, v109
	v_or_b32_e32 v112, s56, v201
	ds_write_b64 v112, v[110:111] offset:12288
	v_and_b32_e32 v110, 8, v242
	v_cmp_eq_u32_e32 vcc, 0, v110
	s_or_b32 s54, s55, s54
	s_bitcmp0_b32 s53, 0
	v_cndmask_b32_e64 v110, 1.0, 0, vcc
	v_pk_fma_f32 v[96:97], v[110:111], v[106:107], v[96:97] op_sel_hi:[0,1,1]
	v_pk_fma_f32 v[94:95], v[110:111], v[108:109], v[94:95] op_sel_hi:[0,1,1]
	s_cselect_b64 vcc, -1, 0
	v_cvt_pk_f16_f32 v96, v96, v97
	v_cvt_pk_f16_f32 v97, v94, v95
	v_cndmask_b32_e32 v94, v201, v202, vcc
	v_or_b32_e32 v94, s54, v94
	v_or_b32_e32 v94, 0x20000, v94
	ds_write_b64 v94, v[96:97]
	s_add_i32 s75, s21, 8
	s_and_b32 s76, s75, 3
	s_cmp_gt_u32 s76, s46
	s_cselect_b32 s77, 2.0, 0
	s_lshr_b32 s75, s75, 2
	s_add_i32 s75, s75, s44
	s_min_u32 s76, s76, s46
	s_lshl_b32 s75, s75, 10
	s_and_b32 s75, s75, 0x1c00
	s_lshl_b32 s76, s76, 18
	s_or_b32 s75, s75, s76
	s_cmp_lt_u32 s21, 24
	s_cselect_b32 s76, 0, 2.0
	s_or_b32 s76, s76, s77
	v_add_u32_e32 v106, s76, v197
	v_add_u32_e32 v107, s76, v198
	v_add_u32_e32 v108, s76, v199
	v_add_u32_e32 v109, s76, v200
	buffer_load_dwordx4 v[126:129], v106, s[4:7], s75 offen sc0 nt sc1
	buffer_load_dwordx4 v[122:125], v107, s[4:7], s75 offen sc0 nt sc1
	buffer_load_dwordx4 v[110:113], v108, s[4:7], s75 offen sc0 nt sc1
	buffer_load_dwordx4 v[106:109], v109, s[4:7], s75 offen sc0 nt sc1
	s_waitcnt lgkmcnt(7)
	v_mfma_f32_32x32x16_f16 v[2:17], v[82:85], v[102:105], v[2:17]
	s_waitcnt lgkmcnt(6)
	v_mfma_f32_32x32x16_f16 v[34:49], v[82:85], v[250:253], v[34:49]
	s_waitcnt lgkmcnt(5)
	v_mfma_f32_32x32x16_f16 v[50:65], v[82:85], v[208:211], v[50:65]
	s_waitcnt lgkmcnt(4)
	v_mfma_f32_32x32x16_f16 v[18:33], v[82:85], v[216:219], v[18:33]
	s_waitcnt lgkmcnt(3)
	v_mfma_f32_32x32x16_f16 v[66:81], v[86:89], v[234:237], v[66:81]
	s_cmp_lg_u32 s38, 3
	s_cbranch_scc1 .LBB1_12
	s_waitcnt lgkmcnt(0)
	s_barrier
.LBB1_12:
	s_lshr_b32 s38, s52, 2
	s_add_i32 s38, s38, s44
	s_lshl_b32 s38, s38, 17
	s_and_b32 s38, s38, 0xe0000
	s_and_b32 s52, s20, 0xc000
	s_or_b32 s38, s38, s52
	v_lshl_add_u64 v[82:83], v[194:195], 0, s[38:39]
	s_add_i32 s38, s41, 11
	s_lshr_b32 s38, s38, 2
	s_add_i32 s38, s38, s44
	v_add_co_u32_e32 v84, vcc, 0x1000, v82
	s_min_u32 s41, s51, s46
	s_lshl_b32 s38, s38, 10
	v_addc_co_u32_e32 v85, vcc, 0, v83, vcc
	s_and_b32 s38, s38, 0x1c00
	s_lshl_b32 s41, s41, 18
	global_load_dwordx4 v[102:105], v[82:83], off
	global_load_dwordx4 v[94:97], v[84:85], off
	v_add_co_u32_e32 v84, vcc, 0x2000, v82
	s_or_b32 s38, s38, s41
	s_nop 0
	v_addc_co_u32_e32 v85, vcc, 0, v83, vcc
	s_cmp_lt_u32 s21, 24
	v_add_co_u32_e32 v86, vcc, 0x3000, v82
	s_cselect_b32 s41, 0, 2.0
	s_nop 0
	v_addc_co_u32_e32 v87, vcc, 0, v83, vcc
	global_load_dwordx4 v[82:85], v[84:85], off
	s_nop 0
	global_load_dwordx4 v[86:89], v[86:87], off
	s_nop 0
	s_nop 0
	s_and_b32 s41, s50, 3
	s_bfe_u32 s38, s50, 0x10002
	s_lshl_b32 s50, s41, 6
	v_lshl_or_b32 v215, s38, 16, v204
	v_xor_b32_e32 v240, s50, v203
	v_add_u32_e32 v226, v215, v240
	ds_read_b128 v[208:211], v226
	ds_read_b128 v[216:219], v226 offset:16384
	ds_read_b128 v[220:223], v226 offset:32768
	ds_read_b128 v[226:229], v226 offset:49152
	v_lshl_add_u32 v241, s38, 14, v206
	v_add_u32_e32 v230, v241, v240
	ds_read_b128 v[230:233], v230
	s_add_i32 s20, s20, 0x18000
	s_and_b32 s20, s20, 0x10000
	s_lshl_b32 s38, s47, 14
	s_or_b32 s20, s20, s38
	s_lshl_b32 s50, s47, 2
	s_waitcnt vmcnt(19)
	v_cvt_pk_f16_f32 v234, v174, v175
	v_cvt_pk_f16_f32 v235, v176, v177
	v_or_b32_e32 v236, s20, v202
	ds_write_b64 v236, v[234:235]
	v_bfe_u32 v234, v205, s50, 1
	v_cmp_eq_u32_e32 vcc, 0, v234
	v_lshrrev_b32_e32 v242, s50, v205
	s_waitcnt vmcnt(17)
	v_cvt_pk_f16_f32 v236, v170, v171
	v_cndmask_b32_e64 v234, 1.0, 0, vcc
	v_pk_fma_f32 v[174:175], v[234:235], v[174:175], 0 op_sel_hi:[0,1,0]
	v_cvt_pk_f16_f32 v237, v172, v173
	v_or_b32_e32 v235, s20, v201
	ds_write_b64 v235, v[236:237] offset:4096
	v_and_b32_e32 v235, 2, v242
	v_cmp_eq_u32_e32 vcc, 0, v235
	s_nop 1
	v_cndmask_b32_e64 v236, 1.0, 0, vcc
	v_pk_fma_f32 v[238:239], v[236:237], v[170:171], v[174:175] op_sel_hi:[0,1,1]
	s_waitcnt lgkmcnt(4)
	v_mfma_f32_32x32x16_f16 v[50:65], v[166:169], v[220:223], v[50:65]
	v_xor_b32_e32 v222, 32, v240
	v_add_u32_e32 v215, v215, v222
	v_fma_f32 v170, v234, v176, 0
	v_fma_f32 v171, v234, v177, 0
	v_fma_f32 v220, v236, v172, v170
	v_fma_f32 v221, v236, v173, v171
	v_add_u32_e32 v254, v241, v222
	v_mfma_f32_32x32x16_f16 v[2:17], v[166:169], v[208:211], v[2:17]
	v_mfma_f32_32x32x16_f16 v[34:49], v[166:169], v[216:219], v[34:49]
	s_waitcnt lgkmcnt(3)
	v_mfma_f32_32x32x16_f16 v[18:33], v[166:169], v[226:229], v[18:33]
	ds_read_b128 v[166:169], v215
	ds_read_b128 v[250:253], v215 offset:16384
	ds_read_b128 v[208:211], v215 offset:32768
	ds_read_b128 v[216:219], v215 offset:49152
	ds_read_b128 v[234:237], v254
	s_waitcnt lgkmcnt(7)
	v_mfma_f32_32x32x16_f16 v[66:81], v[158:161], v[230:233], v[66:81]
	s_bfe_u32 s20, s48, 0x10002
	s_lshl_b32 s48, s20, 16
	s_or_b32 s38, s48, s38
	s_waitcnt vmcnt(17)
	v_cvt_pk_f16_f32 v158, v162, v163
	v_cvt_pk_f16_f32 v159, v164, v165
	v_or_b32_e32 v160, s38, v202
	ds_write_b64 v160, v[158:159] offset:8192
	v_and_b32_e32 v158, 4, v242
	v_cmp_eq_u32_e32 vcc, 0, v158
	s_lshl_b32 s20, s20, 14
	s_nop 0
	v_cndmask_b32_e64 v158, 1.0, 0, vcc
	v_pk_fma_f32 v[160:161], v[158:159], v[162:163], v[238:239] op_sel_hi:[0,1,1]
	v_pk_fma_f32 v[158:159], v[158:159], v[164:165], v[220:221] op_sel_hi:[0,1,1]
	s_waitcnt vmcnt(16)
	v_cvt_pk_f16_f32 v162, v154, v155
	v_cvt_pk_f16_f32 v163, v156, v157
	v_or_b32_e32 v164, s38, v201
	ds_write_b64 v164, v[162:163] offset:12288
	v_and_b32_e32 v162, 8, v242
	v_cmp_eq_u32_e32 vcc, 0, v162
	s_lshl_b32 s38, s47, 12
	s_or_b32 s20, s20, s38
	v_cndmask_b32_e64 v162, 1.0, 0, vcc
	v_pk_fma_f32 v[154:155], v[162:163], v[154:155], v[160:161] op_sel_hi:[0,1,1]
	v_pk_fma_f32 v[156:157], v[162:163], v[156:157], v[158:159] op_sel_hi:[0,1,1]
	v_cvt_pk_f16_f32 v154, v154, v155
	v_cvt_pk_f16_f32 v155, v156, v157
	v_or_b32_e32 v156, s20, v207
	v_or_b32_e32 v156, 0x20000, v156
	ds_write_b64 v156, v[154:155]
	s_cmp_gt_u32 s21, 26
	s_cbranch_scc1 .Lskip_c
	s_add_i32 s75, s21, 9
	s_and_b32 s76, s75, 3
	s_cmp_gt_u32 s76, s46
	s_cselect_b32 s77, 2.0, 0
	s_lshr_b32 s75, s75, 2
	s_add_i32 s75, s75, s44
	s_min_u32 s76, s76, s46
	s_lshl_b32 s75, s75, 10
	s_and_b32 s75, s75, 0x1c00
	s_lshl_b32 s76, s76, 18
	s_or_b32 s75, s75, s76
	s_cmp_lt_u32 s21, 23
	s_cselect_b32 s76, 0, 2.0
	s_or_b32 s76, s76, s77
	v_add_u32_e32 v154, s76, v197
	v_add_u32_e32 v155, s76, v198
	v_add_u32_e32 v156, s76, v199
	v_add_u32_e32 v157, s76, v200
	buffer_load_dwordx4 v[174:177], v154, s[4:7], s75 offen sc0 nt sc1
	buffer_load_dwordx4 v[170:173], v155, s[4:7], s75 offen sc0 nt sc1
	buffer_load_dwordx4 v[162:165], v156, s[4:7], s75 offen sc0 nt sc1
	buffer_load_dwordx4 v[154:157], v157, s[4:7], s75 offen sc0 nt sc1
